# NSA phase: one static s_setprio 1 for waves 4..7 (the younger half), reset at phase end
# speedup vs baseline: 1.0097x; 1.0097x over previous
.Lmy_nsa_nomap:
	v_readfirstlane_b32 s101, v0
	s_nop 3
	s_lshr_b32 s101, s101, 8
	s_cmp_eq_u32 s101, 0
	s_cbranch_scc1 .Lmy_nsa_noprio
	s_setprio 1

.LBB0_930:
	s_setprio 0
	v_readlane_b32 s4, v251, 25
	v_readlane_b32 s8, v251, 29
	v_readlane_b32 s9, v251, 30
	v_readlane_b32 s5, v251, 26
	v_readlane_b32 s6, v251, 27
	v_readlane_b32 s7, v251, 28
	s_mov_b64 s[84:85], s[8:9]
	v_readlane_b32 s92, v252, 62
	v_readlane_b32 s94, v251, 11
	s_mov_b64 s[82:83], s[6:7]
	s_mov_b64 s[80:81], s[4:5]
	v_readlane_b32 s88, v251, 15
	v_readlane_b32 s90, v251, 13
	v_readlane_b32 s93, v252, 63
	v_readlane_b32 s95, v251, 12
	v_readlane_b32 s96, v251, 35
	v_readlane_b32 s10, v251, 31
	v_readlane_b32 s11, v251, 32
	v_readlane_b32 s89, v251, 16
	v_readlane_b32 s91, v251, 14
	v_readlane_b32 s97, v251, 36
